# KV2 A/B loader waves rewritten: 4 register stages in flight (was 2), counted waits, unrolled; plus prep_all block rotation (weights/proj/colsum first)
# baseline (speedup 1.0000x reference)
_Z8prep_all5PArgs:
	s_add_i32 s3, s2, 0x1000
	s_sub_i32 s4, s2, 0xa21
	s_cmpk_lt_u32 s2, 0xa21
	s_cselect_b32 s2, s3, s4
	s_cmpk_gt_i32 s2, 0xfff
	s_mov_b64 s[4:5], -1
	s_cbranch_scc1 .LBB0_3
	s_andn2_b64 vcc, exec, s[4:5]
	s_cbranch_vccz .LBB0_40

.LBB3_63:
	s_and_b64 vcc, exec, s[2:3]
	s_cbranch_vccz .LBB3_66
	v_add_u32_e32 v1, 0xffffff00, v0
	v_ashrrev_i32_e32 v74, 3, v1
	v_and_b32_e32 v4, 7, v0
	v_lshlrev_b32_e32 v4, 4, v4
	v_lshl_add_u32 v150, v74, 11, v4
	v_add_u32_e32 v151, 0x8000, v150
	v_add_u32_e32 v152, 0x10000, v150
	v_add_u32_e32 v153, 0x18000, v150
	v_add_u32_e32 v154, 0x20000, v150
	v_add_u32_e32 v155, 0x28000, v150
	v_add_u32_e32 v156, 0x30000, v150
	v_add_u32_e32 v157, 0x38000, v150
	v_lshlrev_b32_e32 v75, 4, v0
	global_load_dwordx4 v[2:5], v150, s[6:7]
	global_load_dwordx4 v[6:9], v151, s[6:7]
	global_load_dwordx4 v[10:13], v152, s[6:7]
	global_load_dwordx4 v[14:17], v153, s[6:7]
	global_load_dwordx4 v[18:21], v154, s[6:7]
	global_load_dwordx4 v[22:25], v155, s[6:7]
	global_load_dwordx4 v[26:29], v156, s[6:7]
	global_load_dwordx4 v[30:33], v157, s[6:7]
	global_load_dwordx4 v[34:37], v150, s[6:7] offset:128
	global_load_dwordx4 v[38:41], v151, s[6:7] offset:128
	global_load_dwordx4 v[42:45], v152, s[6:7] offset:128
	global_load_dwordx4 v[46:49], v153, s[6:7] offset:128
	global_load_dwordx4 v[50:53], v154, s[6:7] offset:128
	global_load_dwordx4 v[54:57], v155, s[6:7] offset:128
	global_load_dwordx4 v[58:61], v156, s[6:7] offset:128
	global_load_dwordx4 v[62:65], v157, s[6:7] offset:128
	global_load_dwordx4 v[84:87], v150, s[6:7] offset:256
	global_load_dwordx4 v[88:91], v151, s[6:7] offset:256
	global_load_dwordx4 v[92:95], v152, s[6:7] offset:256
	global_load_dwordx4 v[96:99], v153, s[6:7] offset:256
	global_load_dwordx4 v[100:103], v154, s[6:7] offset:256
	global_load_dwordx4 v[104:107], v155, s[6:7] offset:256
	global_load_dwordx4 v[108:111], v156, s[6:7] offset:256
	global_load_dwordx4 v[112:115], v157, s[6:7] offset:256
	global_load_dwordx4 v[116:119], v150, s[6:7] offset:384
	global_load_dwordx4 v[120:123], v151, s[6:7] offset:384
	global_load_dwordx4 v[124:127], v152, s[6:7] offset:384
	global_load_dwordx4 v[128:131], v153, s[6:7] offset:384
	global_load_dwordx4 v[132:135], v154, s[6:7] offset:384
	global_load_dwordx4 v[136:139], v155, s[6:7] offset:384
	global_load_dwordx4 v[140:143], v156, s[6:7] offset:384
	global_load_dwordx4 v[144:147], v157, s[6:7] offset:384
	v_bfe_u32 v76, v0, 2, 1
	v_lshrrev_b32_e32 v1, 6, v1
	s_mov_b32 s0, 0x3ffffe
	v_and_b32_e32 v75, 48, v75
	v_and_or_b32 v1, v1, s0, v76
	v_lshlrev_b32_e32 v68, 6, v74
	s_movk_i32 s1, 0x3c0
	v_lshlrev_b32_e32 v69, 2, v74
	v_and_or_b32 v68, v68, s1, v75
	v_lshlrev_b32_e32 v1, 10, v1
	v_and_b32_e32 v69, 32, v69
	v_bitop3_b32 v1, v68, v1, v69 bitop3:0xde
	v_add_u32_e32 v68, 16, v74
	v_lshrrev_b32_e32 v69, 3, v68
	v_and_or_b32 v69, v69, s0, v76
	v_lshlrev_b32_e32 v70, 6, v68
	v_lshlrev_b32_e32 v68, 2, v68
	v_and_or_b32 v70, v70, s1, v75
	v_lshlrev_b32_e32 v69, 10, v69
	v_and_b32_e32 v68, 32, v68
	v_bitop3_b32 v68, v70, v69, v68 bitop3:0xde
	v_add_u32_e32 v69, 32, v74
	v_lshrrev_b32_e32 v70, 3, v69
	v_and_or_b32 v70, v70, s0, v76
	v_lshlrev_b32_e32 v71, 6, v69
	v_lshlrev_b32_e32 v69, 2, v69
	v_and_or_b32 v71, v71, s1, v75
	v_lshlrev_b32_e32 v70, 10, v70
	v_and_b32_e32 v69, 32, v69
	v_bitop3_b32 v69, v71, v70, v69 bitop3:0xde
	v_add_u32_e32 v70, 48, v74
	v_lshrrev_b32_e32 v71, 3, v70
	v_and_or_b32 v71, v71, s0, v76
	v_lshlrev_b32_e32 v72, 6, v70
	v_lshlrev_b32_e32 v70, 2, v70
	v_and_or_b32 v72, v72, s1, v75
	v_lshlrev_b32_e32 v71, 10, v71
	v_and_b32_e32 v70, 32, v70
	v_bitop3_b32 v70, v72, v71, v70 bitop3:0xde
	v_add_u32_e32 v71, 64, v74
	v_lshrrev_b32_e32 v72, 3, v71
	v_and_or_b32 v72, v72, s0, v76
	v_lshlrev_b32_e32 v73, 6, v71
	v_lshlrev_b32_e32 v71, 2, v71
	v_and_or_b32 v73, v73, s1, v75
	v_lshlrev_b32_e32 v72, 10, v72
	v_and_b32_e32 v71, 32, v71
	v_bitop3_b32 v71, v73, v72, v71 bitop3:0xde
	v_add_u32_e32 v72, 0x50, v74
	v_lshrrev_b32_e32 v73, 3, v72
	v_and_or_b32 v73, v73, s0, v76
	v_lshlrev_b32_e32 v77, 6, v72
	v_lshlrev_b32_e32 v72, 2, v72
	v_and_or_b32 v77, v77, s1, v75
	v_lshlrev_b32_e32 v73, 10, v73
	v_and_b32_e32 v72, 32, v72
	v_bitop3_b32 v72, v77, v73, v72 bitop3:0xde
	v_add_u32_e32 v73, 0x60, v74
	v_lshrrev_b32_e32 v77, 3, v73
	v_and_or_b32 v77, v77, s0, v76
	v_lshlrev_b32_e32 v78, 6, v73
	v_lshlrev_b32_e32 v73, 2, v73
	v_and_or_b32 v78, v78, s1, v75
	v_lshlrev_b32_e32 v77, 10, v77
	v_and_b32_e32 v73, 32, v73
	v_add_u32_e32 v74, 0x70, v74
	v_bitop3_b32 v73, v78, v77, v73 bitop3:0xde
	v_lshrrev_b32_e32 v77, 3, v74
	v_and_or_b32 v76, v77, s0, v76
	v_lshlrev_b32_e32 v77, 6, v74
	v_lshlrev_b32_e32 v74, 2, v74
	v_and_or_b32 v75, v77, s1, v75
	v_lshlrev_b32_e32 v76, 10, v76
	v_and_b32_e32 v74, 32, v74
	v_bitop3_b32 v74, v75, v76, v74 bitop3:0xde
	s_waitcnt vmcnt(24)
	ds_write_b128 v1, v[2:5]
	ds_write_b128 v68, v[6:9]
	ds_write_b128 v69, v[10:13]
	ds_write_b128 v70, v[14:17]
	ds_write_b128 v71, v[18:21]
	ds_write_b128 v72, v[22:25]
	ds_write_b128 v73, v[26:29]
	ds_write_b128 v74, v[30:33]
	global_load_dwordx4 v[2:5], v150, s[6:7] offset:512
	global_load_dwordx4 v[6:9], v151, s[6:7] offset:512
	global_load_dwordx4 v[10:13], v152, s[6:7] offset:512
	global_load_dwordx4 v[14:17], v153, s[6:7] offset:512
	global_load_dwordx4 v[18:21], v154, s[6:7] offset:512
	global_load_dwordx4 v[22:25], v155, s[6:7] offset:512
	global_load_dwordx4 v[26:29], v156, s[6:7] offset:512
	global_load_dwordx4 v[30:33], v157, s[6:7] offset:512
	s_waitcnt lgkmcnt(0)
	s_barrier
	s_waitcnt vmcnt(24)
	ds_write_b128 v1, v[34:37] offset:24576
	ds_write_b128 v68, v[38:41] offset:24576
	ds_write_b128 v69, v[42:45] offset:24576
	ds_write_b128 v70, v[46:49] offset:24576
	ds_write_b128 v71, v[50:53] offset:24576
	ds_write_b128 v72, v[54:57] offset:24576
	ds_write_b128 v73, v[58:61] offset:24576
	ds_write_b128 v74, v[62:65] offset:24576
	global_load_dwordx4 v[34:37], v150, s[6:7] offset:640
	global_load_dwordx4 v[38:41], v151, s[6:7] offset:640
	global_load_dwordx4 v[42:45], v152, s[6:7] offset:640
	global_load_dwordx4 v[46:49], v153, s[6:7] offset:640
	global_load_dwordx4 v[50:53], v154, s[6:7] offset:640
	global_load_dwordx4 v[54:57], v155, s[6:7] offset:640
	global_load_dwordx4 v[58:61], v156, s[6:7] offset:640
	global_load_dwordx4 v[62:65], v157, s[6:7] offset:640
	s_waitcnt lgkmcnt(0)
	s_barrier
	s_waitcnt vmcnt(24)
	ds_write_b128 v1, v[84:87] offset:49152
	ds_write_b128 v68, v[88:91] offset:49152
	ds_write_b128 v69, v[92:95] offset:49152
	ds_write_b128 v70, v[96:99] offset:49152
	ds_write_b128 v71, v[100:103] offset:49152
	ds_write_b128 v72, v[104:107] offset:49152
	ds_write_b128 v73, v[108:111] offset:49152
	ds_write_b128 v74, v[112:115] offset:49152
	global_load_dwordx4 v[84:87], v150, s[6:7] offset:768
	global_load_dwordx4 v[88:91], v151, s[6:7] offset:768
	global_load_dwordx4 v[92:95], v152, s[6:7] offset:768
	global_load_dwordx4 v[96:99], v153, s[6:7] offset:768
	global_load_dwordx4 v[100:103], v154, s[6:7] offset:768
	global_load_dwordx4 v[104:107], v155, s[6:7] offset:768
	global_load_dwordx4 v[108:111], v156, s[6:7] offset:768
	global_load_dwordx4 v[112:115], v157, s[6:7] offset:768
	s_waitcnt lgkmcnt(0)
	s_barrier
	s_waitcnt vmcnt(24)
	ds_write_b128 v1, v[116:119]
	ds_write_b128 v68, v[120:123]
	ds_write_b128 v69, v[124:127]
	ds_write_b128 v70, v[128:131]
	ds_write_b128 v71, v[132:135]
	ds_write_b128 v72, v[136:139]
	ds_write_b128 v73, v[140:143]
	ds_write_b128 v74, v[144:147]
	global_load_dwordx4 v[116:119], v150, s[6:7] offset:896
	global_load_dwordx4 v[120:123], v151, s[6:7] offset:896
	global_load_dwordx4 v[124:127], v152, s[6:7] offset:896
	global_load_dwordx4 v[128:131], v153, s[6:7] offset:896
	global_load_dwordx4 v[132:135], v154, s[6:7] offset:896
	global_load_dwordx4 v[136:139], v155, s[6:7] offset:896
	global_load_dwordx4 v[140:143], v156, s[6:7] offset:896
	global_load_dwordx4 v[144:147], v157, s[6:7] offset:896
	s_waitcnt lgkmcnt(0)
	s_barrier
	s_waitcnt vmcnt(24)
	ds_write_b128 v1, v[2:5] offset:24576
	ds_write_b128 v68, v[6:9] offset:24576
	ds_write_b128 v69, v[10:13] offset:24576
	ds_write_b128 v70, v[14:17] offset:24576
	ds_write_b128 v71, v[18:21] offset:24576
	ds_write_b128 v72, v[22:25] offset:24576
	ds_write_b128 v73, v[26:29] offset:24576
	ds_write_b128 v74, v[30:33] offset:24576
	global_load_dwordx4 v[2:5], v150, s[6:7] offset:1024
	global_load_dwordx4 v[6:9], v151, s[6:7] offset:1024
	global_load_dwordx4 v[10:13], v152, s[6:7] offset:1024
	global_load_dwordx4 v[14:17], v153, s[6:7] offset:1024
	global_load_dwordx4 v[18:21], v154, s[6:7] offset:1024
	global_load_dwordx4 v[22:25], v155, s[6:7] offset:1024
	global_load_dwordx4 v[26:29], v156, s[6:7] offset:1024
	global_load_dwordx4 v[30:33], v157, s[6:7] offset:1024
	s_waitcnt lgkmcnt(0)
	s_barrier
	s_waitcnt vmcnt(24)
	ds_write_b128 v1, v[34:37] offset:49152
	ds_write_b128 v68, v[38:41] offset:49152
	ds_write_b128 v69, v[42:45] offset:49152
	ds_write_b128 v70, v[46:49] offset:49152
	ds_write_b128 v71, v[50:53] offset:49152
	ds_write_b128 v72, v[54:57] offset:49152
	ds_write_b128 v73, v[58:61] offset:49152
	ds_write_b128 v74, v[62:65] offset:49152
	global_load_dwordx4 v[34:37], v150, s[6:7] offset:1152
	global_load_dwordx4 v[38:41], v151, s[6:7] offset:1152
	global_load_dwordx4 v[42:45], v152, s[6:7] offset:1152
	global_load_dwordx4 v[46:49], v153, s[6:7] offset:1152
	global_load_dwordx4 v[50:53], v154, s[6:7] offset:1152
	global_load_dwordx4 v[54:57], v155, s[6:7] offset:1152
	global_load_dwordx4 v[58:61], v156, s[6:7] offset:1152
	global_load_dwordx4 v[62:65], v157, s[6:7] offset:1152
	s_waitcnt lgkmcnt(0)
	s_barrier
	s_waitcnt vmcnt(24)
	ds_write_b128 v1, v[84:87]
	ds_write_b128 v68, v[88:91]
	ds_write_b128 v69, v[92:95]
	ds_write_b128 v70, v[96:99]
	ds_write_b128 v71, v[100:103]
	ds_write_b128 v72, v[104:107]
	ds_write_b128 v73, v[108:111]
	ds_write_b128 v74, v[112:115]
	global_load_dwordx4 v[84:87], v150, s[6:7] offset:1280
	global_load_dwordx4 v[88:91], v151, s[6:7] offset:1280
	global_load_dwordx4 v[92:95], v152, s[6:7] offset:1280
	global_load_dwordx4 v[96:99], v153, s[6:7] offset:1280
	global_load_dwordx4 v[100:103], v154, s[6:7] offset:1280
	global_load_dwordx4 v[104:107], v155, s[6:7] offset:1280
	global_load_dwordx4 v[108:111], v156, s[6:7] offset:1280
	global_load_dwordx4 v[112:115], v157, s[6:7] offset:1280
	s_waitcnt lgkmcnt(0)
	s_barrier
	s_waitcnt vmcnt(24)
	ds_write_b128 v1, v[116:119] offset:24576
	ds_write_b128 v68, v[120:123] offset:24576
	ds_write_b128 v69, v[124:127] offset:24576
	ds_write_b128 v70, v[128:131] offset:24576
	ds_write_b128 v71, v[132:135] offset:24576
	ds_write_b128 v72, v[136:139] offset:24576
	ds_write_b128 v73, v[140:143] offset:24576
	ds_write_b128 v74, v[144:147] offset:24576
	global_load_dwordx4 v[116:119], v150, s[6:7] offset:1408
	global_load_dwordx4 v[120:123], v151, s[6:7] offset:1408
	global_load_dwordx4 v[124:127], v152, s[6:7] offset:1408
	global_load_dwordx4 v[128:131], v153, s[6:7] offset:1408
	global_load_dwordx4 v[132:135], v154, s[6:7] offset:1408
	global_load_dwordx4 v[136:139], v155, s[6:7] offset:1408
	global_load_dwordx4 v[140:143], v156, s[6:7] offset:1408
	global_load_dwordx4 v[144:147], v157, s[6:7] offset:1408
	s_waitcnt lgkmcnt(0)
	s_barrier
	s_waitcnt vmcnt(24)
	ds_write_b128 v1, v[2:5] offset:49152
	ds_write_b128 v68, v[6:9] offset:49152
	ds_write_b128 v69, v[10:13] offset:49152
	ds_write_b128 v70, v[14:17] offset:49152
	ds_write_b128 v71, v[18:21] offset:49152
	ds_write_b128 v72, v[22:25] offset:49152
	ds_write_b128 v73, v[26:29] offset:49152
	ds_write_b128 v74, v[30:33] offset:49152
	global_load_dwordx4 v[2:5], v150, s[6:7] offset:1536
	global_load_dwordx4 v[6:9], v151, s[6:7] offset:1536
	global_load_dwordx4 v[10:13], v152, s[6:7] offset:1536
	global_load_dwordx4 v[14:17], v153, s[6:7] offset:1536
	global_load_dwordx4 v[18:21], v154, s[6:7] offset:1536
	global_load_dwordx4 v[22:25], v155, s[6:7] offset:1536
	global_load_dwordx4 v[26:29], v156, s[6:7] offset:1536
	global_load_dwordx4 v[30:33], v157, s[6:7] offset:1536
	s_waitcnt lgkmcnt(0)
	s_barrier
	s_waitcnt vmcnt(24)
	ds_write_b128 v1, v[34:37]
	ds_write_b128 v68, v[38:41]
	ds_write_b128 v69, v[42:45]
	ds_write_b128 v70, v[46:49]
	ds_write_b128 v71, v[50:53]
	ds_write_b128 v72, v[54:57]
	ds_write_b128 v73, v[58:61]
	ds_write_b128 v74, v[62:65]
	global_load_dwordx4 v[34:37], v150, s[6:7] offset:1664
	global_load_dwordx4 v[38:41], v151, s[6:7] offset:1664
	global_load_dwordx4 v[42:45], v152, s[6:7] offset:1664
	global_load_dwordx4 v[46:49], v153, s[6:7] offset:1664
	global_load_dwordx4 v[50:53], v154, s[6:7] offset:1664
	global_load_dwordx4 v[54:57], v155, s[6:7] offset:1664
	global_load_dwordx4 v[58:61], v156, s[6:7] offset:1664
	global_load_dwordx4 v[62:65], v157, s[6:7] offset:1664
	s_waitcnt lgkmcnt(0)
	s_barrier
	s_waitcnt vmcnt(24)
	ds_write_b128 v1, v[84:87] offset:24576
	ds_write_b128 v68, v[88:91] offset:24576
	ds_write_b128 v69, v[92:95] offset:24576
	ds_write_b128 v70, v[96:99] offset:24576
	ds_write_b128 v71, v[100:103] offset:24576
	ds_write_b128 v72, v[104:107] offset:24576
	ds_write_b128 v73, v[108:111] offset:24576
	ds_write_b128 v74, v[112:115] offset:24576
	global_load_dwordx4 v[84:87], v150, s[6:7] offset:1792
	global_load_dwordx4 v[88:91], v151, s[6:7] offset:1792
	global_load_dwordx4 v[92:95], v152, s[6:7] offset:1792
	global_load_dwordx4 v[96:99], v153, s[6:7] offset:1792
	global_load_dwordx4 v[100:103], v154, s[6:7] offset:1792
	global_load_dwordx4 v[104:107], v155, s[6:7] offset:1792
	global_load_dwordx4 v[108:111], v156, s[6:7] offset:1792
	global_load_dwordx4 v[112:115], v157, s[6:7] offset:1792
	s_waitcnt lgkmcnt(0)
	s_barrier
	s_waitcnt vmcnt(24)
	ds_write_b128 v1, v[116:119] offset:49152
	ds_write_b128 v68, v[120:123] offset:49152
	ds_write_b128 v69, v[124:127] offset:49152
	ds_write_b128 v70, v[128:131] offset:49152
	ds_write_b128 v71, v[132:135] offset:49152
	ds_write_b128 v72, v[136:139] offset:49152
	ds_write_b128 v73, v[140:143] offset:49152
	ds_write_b128 v74, v[144:147] offset:49152
	global_load_dwordx4 v[116:119], v150, s[6:7] offset:1920
	global_load_dwordx4 v[120:123], v151, s[6:7] offset:1920
	global_load_dwordx4 v[124:127], v152, s[6:7] offset:1920
	global_load_dwordx4 v[128:131], v153, s[6:7] offset:1920
	global_load_dwordx4 v[132:135], v154, s[6:7] offset:1920
	global_load_dwordx4 v[136:139], v155, s[6:7] offset:1920
	global_load_dwordx4 v[140:143], v156, s[6:7] offset:1920
	global_load_dwordx4 v[144:147], v157, s[6:7] offset:1920
	s_waitcnt lgkmcnt(0)
	s_barrier
	s_waitcnt vmcnt(24)
	ds_write_b128 v1, v[2:5]
	ds_write_b128 v68, v[6:9]
	ds_write_b128 v69, v[10:13]
	ds_write_b128 v70, v[14:17]
	ds_write_b128 v71, v[18:21]
	ds_write_b128 v72, v[22:25]
	ds_write_b128 v73, v[26:29]
	ds_write_b128 v74, v[30:33]
	s_waitcnt lgkmcnt(0)
	s_barrier
	s_waitcnt vmcnt(16)
	ds_write_b128 v1, v[34:37] offset:24576
	ds_write_b128 v68, v[38:41] offset:24576
	ds_write_b128 v69, v[42:45] offset:24576
	ds_write_b128 v70, v[46:49] offset:24576
	ds_write_b128 v71, v[50:53] offset:24576
	ds_write_b128 v72, v[54:57] offset:24576
	ds_write_b128 v73, v[58:61] offset:24576
	ds_write_b128 v74, v[62:65] offset:24576
	s_waitcnt lgkmcnt(0)
	s_barrier
	s_waitcnt vmcnt(8)
	ds_write_b128 v1, v[84:87] offset:49152
	ds_write_b128 v68, v[88:91] offset:49152
	ds_write_b128 v69, v[92:95] offset:49152
	ds_write_b128 v70, v[96:99] offset:49152
	ds_write_b128 v71, v[100:103] offset:49152
	ds_write_b128 v72, v[104:107] offset:49152
	ds_write_b128 v73, v[108:111] offset:49152
	ds_write_b128 v74, v[112:115] offset:49152
	s_waitcnt lgkmcnt(0)
	s_barrier
	s_waitcnt vmcnt(0)
	ds_write_b128 v1, v[116:119]
	ds_write_b128 v68, v[120:123]
	ds_write_b128 v69, v[124:127]
	ds_write_b128 v70, v[128:131]
	ds_write_b128 v71, v[132:135]
	ds_write_b128 v72, v[136:139]
	ds_write_b128 v73, v[140:143]
	ds_write_b128 v74, v[144:147]
	s_waitcnt lgkmcnt(0)
	s_barrier

.LBB3_67:
	v_add_u32_e32 v1, 0xfffffe80, v0
	s_lshl_b32 s0, s24, 17
	v_ashrrev_i32_e32 v36, 3, v1
	s_add_u32 s28, s4, s0
	s_addc_u32 s29, s5, 0
	v_and_b32_e32 v4, 7, v0
	v_lshlrev_b32_e32 v4, 4, v4
	v_lshl_add_u32 v150, v36, 11, v4
	v_add_u32_e32 v151, 0x8000, v150
	v_add_u32_e32 v152, 0x10000, v150
	v_add_u32_e32 v153, 0x18000, v150
	v_lshlrev_b32_e32 v37, 4, v0
	global_load_dwordx4 v[2:5], v150, s[28:29]
	global_load_dwordx4 v[6:9], v151, s[28:29]
	global_load_dwordx4 v[10:13], v152, s[28:29]
	global_load_dwordx4 v[14:17], v153, s[28:29]
	global_load_dwordx4 v[18:21], v150, s[28:29] offset:128
	global_load_dwordx4 v[22:25], v151, s[28:29] offset:128
	global_load_dwordx4 v[26:29], v152, s[28:29] offset:128
	global_load_dwordx4 v[30:33], v153, s[28:29] offset:128
	global_load_dwordx4 v[50:53], v150, s[28:29] offset:256
	global_load_dwordx4 v[54:57], v151, s[28:29] offset:256
	global_load_dwordx4 v[58:61], v152, s[28:29] offset:256
	global_load_dwordx4 v[62:65], v153, s[28:29] offset:256
	global_load_dwordx4 v[66:69], v150, s[28:29] offset:384
	global_load_dwordx4 v[70:73], v151, s[28:29] offset:384
	global_load_dwordx4 v[74:77], v152, s[28:29] offset:384
	global_load_dwordx4 v[78:81], v153, s[28:29] offset:384
	v_lshlrev_b32_e32 v38, 6, v36
	v_lshlrev_b32_e32 v39, 2, v36
	v_add_u32_e32 v40, 16, v36
	v_add_u32_e32 v43, 32, v36
	v_add_u32_e32 v36, 48, v36
	v_bfe_u32 v0, v0, 2, 1
	v_lshrrev_b32_e32 v1, 6, v1
	s_mov_b32 s0, 0x3ffffe
	v_lshrrev_b32_e32 v41, 3, v40
	v_lshrrev_b32_e32 v44, 3, v43
	v_lshrrev_b32_e32 v46, 3, v36
	v_and_b32_e32 v37, 48, v37
	v_and_or_b32 v1, v1, s0, v0
	s_movk_i32 s5, 0x3c0
	v_and_or_b32 v41, v41, s0, v0
	v_lshlrev_b32_e32 v42, 6, v40
	v_and_or_b32 v44, v44, s0, v0
	v_lshlrev_b32_e32 v45, 6, v43
	v_and_or_b32 v0, v46, s0, v0
	v_lshlrev_b32_e32 v46, 6, v36
	v_and_or_b32 v38, v38, s5, v37
	v_and_or_b32 v42, v42, s5, v37
	v_lshlrev_b32_e32 v40, 2, v40
	v_and_or_b32 v45, v45, s5, v37
	v_lshlrev_b32_e32 v43, 2, v43
	v_and_or_b32 v37, v46, s5, v37
	v_lshlrev_b32_e32 v46, 10, v0
	v_lshlrev_b32_e32 v0, 2, v36
	v_lshlrev_b32_e32 v1, 10, v1
	v_and_b32_e32 v39, 32, v39
	v_lshlrev_b32_e32 v41, 10, v41
	v_and_b32_e32 v40, 32, v40
	v_lshlrev_b32_e32 v44, 10, v44
	v_and_b32_e32 v43, 32, v43
	v_and_b32_e32 v47, 32, v0
	s_mov_b32 s1, 0
	v_bitop3_b32 v0, v1, v38, v39 bitop3:0xf6
	v_bitop3_b32 v1, v41, v42, v40 bitop3:0xf6
	v_bitop3_b32 v36, v44, v45, v43 bitop3:0xf6
	v_bitop3_b32 v37, v46, v37, v47 bitop3:0xf6
	v_add_u32_e32 v0, 0x4000, v0
	v_add_u32_e32 v1, 0x4000, v1
	v_add_u32_e32 v36, 0x4000, v36
	v_add_u32_e32 v37, 0x4000, v37
	s_waitcnt vmcnt(12)
	ds_write_b128 v0, v[2:5]
	ds_write_b128 v1, v[6:9]
	ds_write_b128 v36, v[10:13]
	ds_write_b128 v37, v[14:17]
	global_load_dwordx4 v[2:5], v150, s[28:29] offset:512
	global_load_dwordx4 v[6:9], v151, s[28:29] offset:512
	global_load_dwordx4 v[10:13], v152, s[28:29] offset:512
	global_load_dwordx4 v[14:17], v153, s[28:29] offset:512
	s_waitcnt lgkmcnt(0)
	s_barrier
	s_waitcnt vmcnt(12)
	ds_write_b128 v0, v[18:21] offset:24576
	ds_write_b128 v1, v[22:25] offset:24576
	ds_write_b128 v36, v[26:29] offset:24576
	ds_write_b128 v37, v[30:33] offset:24576
	global_load_dwordx4 v[18:21], v150, s[28:29] offset:640
	global_load_dwordx4 v[22:25], v151, s[28:29] offset:640
	global_load_dwordx4 v[26:29], v152, s[28:29] offset:640
	global_load_dwordx4 v[30:33], v153, s[28:29] offset:640
	s_waitcnt lgkmcnt(0)
	s_barrier
	s_waitcnt vmcnt(12)
	ds_write_b128 v0, v[50:53] offset:49152
	ds_write_b128 v1, v[54:57] offset:49152
	ds_write_b128 v36, v[58:61] offset:49152
	ds_write_b128 v37, v[62:65] offset:49152
	global_load_dwordx4 v[50:53], v150, s[28:29] offset:768
	global_load_dwordx4 v[54:57], v151, s[28:29] offset:768
	global_load_dwordx4 v[58:61], v152, s[28:29] offset:768
	global_load_dwordx4 v[62:65], v153, s[28:29] offset:768
	s_waitcnt lgkmcnt(0)
	s_barrier
	s_waitcnt vmcnt(12)
	ds_write_b128 v0, v[66:69]
	ds_write_b128 v1, v[70:73]
	ds_write_b128 v36, v[74:77]
	ds_write_b128 v37, v[78:81]
	global_load_dwordx4 v[66:69], v150, s[28:29] offset:896
	global_load_dwordx4 v[70:73], v151, s[28:29] offset:896
	global_load_dwordx4 v[74:77], v152, s[28:29] offset:896
	global_load_dwordx4 v[78:81], v153, s[28:29] offset:896
	s_waitcnt lgkmcnt(0)
	s_barrier
	s_waitcnt vmcnt(12)
	ds_write_b128 v0, v[2:5] offset:24576
	ds_write_b128 v1, v[6:9] offset:24576
	ds_write_b128 v36, v[10:13] offset:24576
	ds_write_b128 v37, v[14:17] offset:24576
	global_load_dwordx4 v[2:5], v150, s[28:29] offset:1024
	global_load_dwordx4 v[6:9], v151, s[28:29] offset:1024
	global_load_dwordx4 v[10:13], v152, s[28:29] offset:1024
	global_load_dwordx4 v[14:17], v153, s[28:29] offset:1024
	s_waitcnt lgkmcnt(0)
	s_barrier
	s_waitcnt vmcnt(12)
	ds_write_b128 v0, v[18:21] offset:49152
	ds_write_b128 v1, v[22:25] offset:49152
	ds_write_b128 v36, v[26:29] offset:49152
	ds_write_b128 v37, v[30:33] offset:49152
	global_load_dwordx4 v[18:21], v150, s[28:29] offset:1152
	global_load_dwordx4 v[22:25], v151, s[28:29] offset:1152
	global_load_dwordx4 v[26:29], v152, s[28:29] offset:1152
	global_load_dwordx4 v[30:33], v153, s[28:29] offset:1152
	s_waitcnt lgkmcnt(0)
	s_barrier
	s_waitcnt vmcnt(12)
	ds_write_b128 v0, v[50:53]
	ds_write_b128 v1, v[54:57]
	ds_write_b128 v36, v[58:61]
	ds_write_b128 v37, v[62:65]
	global_load_dwordx4 v[50:53], v150, s[28:29] offset:1280
	global_load_dwordx4 v[54:57], v151, s[28:29] offset:1280
	global_load_dwordx4 v[58:61], v152, s[28:29] offset:1280
	global_load_dwordx4 v[62:65], v153, s[28:29] offset:1280
	s_waitcnt lgkmcnt(0)
	s_barrier
	s_waitcnt vmcnt(12)
	ds_write_b128 v0, v[66:69] offset:24576
	ds_write_b128 v1, v[70:73] offset:24576
	ds_write_b128 v36, v[74:77] offset:24576
	ds_write_b128 v37, v[78:81] offset:24576
	global_load_dwordx4 v[66:69], v150, s[28:29] offset:1408
	global_load_dwordx4 v[70:73], v151, s[28:29] offset:1408
	global_load_dwordx4 v[74:77], v152, s[28:29] offset:1408
	global_load_dwordx4 v[78:81], v153, s[28:29] offset:1408
	s_waitcnt lgkmcnt(0)
	s_barrier
	s_waitcnt vmcnt(12)
	ds_write_b128 v0, v[2:5] offset:49152
	ds_write_b128 v1, v[6:9] offset:49152
	ds_write_b128 v36, v[10:13] offset:49152
	ds_write_b128 v37, v[14:17] offset:49152
	global_load_dwordx4 v[2:5], v150, s[28:29] offset:1536
	global_load_dwordx4 v[6:9], v151, s[28:29] offset:1536
	global_load_dwordx4 v[10:13], v152, s[28:29] offset:1536
	global_load_dwordx4 v[14:17], v153, s[28:29] offset:1536
	s_waitcnt lgkmcnt(0)
	s_barrier
	s_waitcnt vmcnt(12)
	ds_write_b128 v0, v[18:21]
	ds_write_b128 v1, v[22:25]
	ds_write_b128 v36, v[26:29]
	ds_write_b128 v37, v[30:33]
	global_load_dwordx4 v[18:21], v150, s[28:29] offset:1664
	global_load_dwordx4 v[22:25], v151, s[28:29] offset:1664
	global_load_dwordx4 v[26:29], v152, s[28:29] offset:1664
	global_load_dwordx4 v[30:33], v153, s[28:29] offset:1664
	s_waitcnt lgkmcnt(0)
	s_barrier
	s_waitcnt vmcnt(12)
	ds_write_b128 v0, v[50:53] offset:24576
	ds_write_b128 v1, v[54:57] offset:24576
	ds_write_b128 v36, v[58:61] offset:24576
	ds_write_b128 v37, v[62:65] offset:24576
	global_load_dwordx4 v[50:53], v150, s[28:29] offset:1792
	global_load_dwordx4 v[54:57], v151, s[28:29] offset:1792
	global_load_dwordx4 v[58:61], v152, s[28:29] offset:1792
	global_load_dwordx4 v[62:65], v153, s[28:29] offset:1792
	s_waitcnt lgkmcnt(0)
	s_barrier
	s_waitcnt vmcnt(12)
	ds_write_b128 v0, v[66:69] offset:49152
	ds_write_b128 v1, v[70:73] offset:49152
	ds_write_b128 v36, v[74:77] offset:49152
	ds_write_b128 v37, v[78:81] offset:49152
	global_load_dwordx4 v[66:69], v150, s[28:29] offset:1920
	global_load_dwordx4 v[70:73], v151, s[28:29] offset:1920
	global_load_dwordx4 v[74:77], v152, s[28:29] offset:1920
	global_load_dwordx4 v[78:81], v153, s[28:29] offset:1920
	s_waitcnt lgkmcnt(0)
	s_barrier
	s_waitcnt vmcnt(12)
	ds_write_b128 v0, v[2:5]
	ds_write_b128 v1, v[6:9]
	ds_write_b128 v36, v[10:13]
	ds_write_b128 v37, v[14:17]
	s_waitcnt lgkmcnt(0)
	s_barrier
	s_waitcnt vmcnt(8)
	ds_write_b128 v0, v[18:21] offset:24576
	ds_write_b128 v1, v[22:25] offset:24576
	ds_write_b128 v36, v[26:29] offset:24576
	ds_write_b128 v37, v[30:33] offset:24576
	s_waitcnt lgkmcnt(0)
	s_barrier
	s_waitcnt vmcnt(4)
	ds_write_b128 v0, v[50:53] offset:49152
	ds_write_b128 v1, v[54:57] offset:49152
	ds_write_b128 v36, v[58:61] offset:49152
	ds_write_b128 v37, v[62:65] offset:49152
	s_waitcnt lgkmcnt(0)
	s_barrier
	s_waitcnt vmcnt(0)
	ds_write_b128 v0, v[66:69]
	ds_write_b128 v1, v[70:73]
	ds_write_b128 v36, v[74:77]
	ds_write_b128 v37, v[78:81]
	s_waitcnt lgkmcnt(0)
	s_barrier
